# hosted conversion split moved to XS=22528 (P4 11 items per wave, P6-idle CUs 18 per wave)
# baseline (speedup 1.0000x reference)
; #define LAS __attribute__((address_space(3)))
; #define LAS __attribute__((address_space(3)))
;     LAS unsigned* scr = (LAS unsigned*)(lds + wave * 16384);
;     WItem d0, d1; WRegs R0, R1;
;     constexpr int KB_ = DM / 32;
;     constexpr int NALL = EARLY ? KB_ * (INW / 128) : KB_ * (DM / 128) + KB_ * (CW / 128) + KB_ * (2 * CW / 128) + (CW / 32) * (DM / 128) + KB_ * (DFF2 / 128) + (DFF / 32) * (DM / 128);
;     const int hi_all = it_hi < NALL ? it_hi : NALL, total = hi_all - it_lo, nwgs = NGW / NWAVES, chunk = (((total + nwgs - 1) / nwgs) + NWAVES - 1) / NWAVES * NWAVES;
;     int it = it_lo + (gw / NWAVES) * chunk + (gw % NWAVES); const int wend0 = it_lo + (gw / NWAVES + 1) * chunk, wend = wend0 < hi_all ? wend0 : hi_all;
; __global__ void __launch_bounds__(NWAVES * 64, 2) mk_fwd(Args args) {
;     ...
;         const int NCONV = (CONV_OVERLAP && G >= 128) ? 51 : 0;
;         if (bx < NCONV) convert_weights<false, true>(P, lds, bx * NWAVES + wave, NCONV * NWAVES, wave, lane, 0, (CONV_OVERLAP && G >= 192) ? LATE_SPLIT : 0x7fffffff);
;         else {
;             sb_phase(lds, PROJ, (bf16*)(ws + WS_MIX), (const float*)(ws + WS_RSB), P.sbo_norm, bx - NCONV, G - NCONV, tid);
;             ret_out_phase(lds, PROJ, (bf16*)(ws + WS_MIX), (const bf16*)(ws + WS_ST), P.ret_norm, bx - NCONV, G - NCONV, tid);
;         }
;         if (NCONV == 0) convert_weights<false>(P, lds, gw, NGW, wave, lane);
.LBB0_519:
	s_mov_b32 s98, 0
	s_mov_b32 s99, 0
	s_mov_b32 s100, s80
	s_mov_b32 s101, s56
	s_mov_b32 s0, 0x9900
	s_cmp_eq_u32 s80, 0x100
	s_cselect_b32 s1, 1, 0
	s_cmp_gt_i32 s75, 6
	s_cselect_b32 s1, s1, 0
	s_cmp_lg_u32 s1, 0
	s_cselect_b32 s0, 0x5800, s0
	v_writelane_b32 v255, s0, 2
	s_mov_b32 s0, 0
	v_writelane_b32 v255, s0, 3

; #define LAS __attribute__((address_space(3)))
; #define LAS __attribute__((address_space(3)))
;     LAS unsigned* scr = (LAS unsigned*)(lds + wave * 16384);
;     WItem d0, d1; WRegs R0, R1;
;     constexpr int KB_ = DM / 32;
;     constexpr int NALL = EARLY ? KB_ * (INW / 128) : KB_ * (DM / 128) + KB_ * (CW / 128) + KB_ * (2 * CW / 128) + (CW / 32) * (DM / 128) + KB_ * (DFF2 / 128) + (DFF / 32) * (DM / 128);
;     const int hi_all = it_hi < NALL ? it_hi : NALL, total = hi_all - it_lo, nwgs = NGW / NWAVES, chunk = (((total + nwgs - 1) / nwgs) + NWAVES - 1) / NWAVES * NWAVES;
;     int it = it_lo + (gw / NWAVES) * chunk + (gw % NWAVES); const int wend0 = it_lo + (gw / NWAVES + 1) * chunk, wend = wend0 < hi_all ? wend0 : hi_all;
; __global__ void __launch_bounds__(NWAVES * 64, 2) mk_fwd(Args args) {
;     ...
;         if (CONV_OVERLAP && G >= 192 && bx >= G / 2 + 8) { __syncthreads(); convert_weights<false, true>(P, lds, (bx - (G / 2 + 8)) * NWAVES + wave, (G - (G / 2 + 8)) * NWAVES, wave, lane, LATE_SPLIT, 0x7fffffff); }
.LBB0_925:
	s_cmpk_lt_i32 s2, 0x88
	s_cbranch_scc1 .Lp6_hook_done
	s_cmp_lg_u32 s80, 0x100
	s_cbranch_scc1 .Lp6_hook_done
	s_cmp_gt_i32 s74, 4
	s_cbranch_scc1 .Lp6_hook_done
	s_cmp_lt_i32 s75, 7
	s_cbranch_scc1 .Lp6_hook_done
	v_writelane_b32 v255, s8, 8
	v_writelane_b32 v255, s9, 9
	v_writelane_b32 v255, s12, 10
	v_writelane_b32 v255, s16, 11
	v_writelane_b32 v255, s18, 12
	v_writelane_b32 v255, s19, 13
	v_writelane_b32 v255, s20, 14
	v_writelane_b32 v255, s21, 15
	v_writelane_b32 v255, s23, 16
	v_writelane_b32 v255, s24, 17
	v_writelane_b32 v255, s26, 18
	v_writelane_b32 v255, s34, 19
	v_readlane_b32 s70, v254, 0
	v_readlane_b32 s71, v254, 1
	v_and_b32_e32 v1, 63, v0
	v_readfirstlane_b32 s101, v0
	s_sub_u32 s100, s2, 0x88
	s_lshl_b32 s100, s100, 3
	s_sub_u32 s70, s70, 0xc0
	s_subb_u32 s71, s71, 0
	s_lshr_b32 s101, s101, 6
	s_add_u32 s101, s101, s100
	s_mov_b32 s100, 120
	s_mov_b32 s0, 0x4100
	v_writelane_b32 v255, s0, 2
	s_mov_b32 s0, 0x5800
	v_writelane_b32 v255, s0, 3
	s_mov_b32 s98, 1
	s_mov_b32 s99, 1
	s_mov_b64 s[4:5], -1
	s_branch .Lp4_conv_entry
